# attention row-max cross-half exchange by v_permlane32_swap instead of ds_bpermute; P11 wave sum by DPP adds + permlane16/32 swaps instead of six serialized ds_bpermute
# baseline (speedup 1.0000x reference)
; __device__ __forceinline__ void unit(LAS unsigned char* lds, const bf16* __restrict__ Q, const bf16* __restrict__ Kp, const bf16* __restrict__ VT, const float* __restrict__ rel, bf16* mix, float* ssa, int b, int h, int u) {
;     ...
;             float mx = max32(p0, p1); mx = fmaxf(mx, __shfl_xor(mx, 32));
;             if (first || __any(mx > THR)) {
;                 const float dl = first ? mx : fmaxf(mx, 0.f); mrun += dl;
;                 const float corr = first ? 1.0f : __builtin_amdgcn_exp2f(-dl); first = false;
; #pragma unroll
;                 for (int r = 0; r < 16; ++r) { p0[r] -= dl; p1[r] -= dl; o0[r] *= corr; o1[r] *= corr; cfarv[r] = cfar - mrun; }
.LBB5_988:
	s_nop 0
	s_nop 15
	s_nop 7
	s_xor_b64 s[42:43], s[40:41], -1
	v_max3_f32 v2, v98, v99, v100
	v_max3_f32 v16, v101, v102, v103
	v_max3_f32 v17, v104, v105, v106
	v_max3_f32 v192, v107, v108, v109
	s_nop 0
	v_max3_f32 v2, v2, v110, v111
	v_max3_f32 v16, v16, v112, v113
	v_max3_f32 v17, v17, v82, v83
	v_max3_f32 v192, v192, v84, v85
	s_nop 0
	v_max3_f32 v2, v2, v86, v87
	v_max3_f32 v16, v16, v88, v89
	v_max3_f32 v17, v17, v90, v91
	v_max3_f32 v192, v192, v92, v93
	s_nop 0
	v_max3_f32 v2, v2, v94, v95
	v_max3_f32 v16, v16, v96, v97
	s_nop 0
	v_max3_f32 v2, v2, v16, v17
	s_nop 0
	v_max3_f32 v2, v2, v192, v192
	s_nop 0
	v_max_f32_e32 v2, v2, v2
	v_mov_b32_e32 v16, v2
	s_and_b64 vcc, exec, s[42:43]
	s_nop 1
	v_permlane32_swap_b32 v16, v2
	s_waitcnt lgkmcnt(0)
	v_max_f32_e32 v16, v2, v16
	s_cbranch_vccz .LBB5_1000
	v_cmp_lt_f32_e32 vcc, s17, v16
	s_mov_b64 s[46:47], 0
	s_mov_b64 s[42:43], 0
	s_cbranch_vccz .LBB5_991
	v_max_f32_e32 v2, v16, v16
	v_max_f32_e32 v2, 0, v2
	s_mov_b64 s[42:43], -1

; __device__ __forceinline__ void unit(LAS unsigned char* lds, const bf16* __restrict__ Q, const bf16* __restrict__ Kp, const bf16* __restrict__ VT, const float* __restrict__ rel, bf16* mix, float* ssa, int b, int h, int u) {
;     ...
;             float mx = max32(p0, p1); mx = fmaxf(mx, __shfl_xor(mx, 32));
;             if (first || __any(mx > THR)) {
;                 const float dl = first ? mx : fmaxf(mx, 0.f); mrun += dl;
;                 const float corr = first ? 1.0f : __builtin_amdgcn_exp2f(-dl); first = false;
; #pragma unroll
;                 for (int r = 0; r < 16; ++r) { p0[r] -= dl; p1[r] -= dl; o0[r] *= corr; o1[r] *= corr; cfarv[r] = cfar - mrun; }
.LBB5_1024:
	s_nop 0
	s_nop 15
	s_nop 7
	s_xor_b64 s[40:41], s[38:39], -1
	v_max3_f32 v2, v98, v99, v100
	v_max3_f32 v16, v101, v102, v103
	v_max3_f32 v17, v104, v105, v106
	v_max3_f32 v189, v107, v108, v109
	s_nop 0
	v_max3_f32 v2, v2, v110, v111
	v_max3_f32 v16, v16, v112, v113
	v_max3_f32 v17, v17, v82, v83
	v_max3_f32 v189, v189, v84, v85
	s_nop 0
	v_max3_f32 v2, v2, v86, v87
	v_max3_f32 v16, v16, v88, v89
	v_max3_f32 v17, v17, v90, v91
	v_max3_f32 v189, v189, v92, v93
	s_nop 0
	v_max3_f32 v2, v2, v94, v95
	v_max3_f32 v16, v16, v96, v97
	s_nop 0
	v_max3_f32 v2, v2, v16, v17
	s_nop 0
	v_max3_f32 v2, v2, v189, v189
	s_nop 0
	v_max_f32_e32 v2, v2, v2
	v_mov_b32_e32 v16, v2
	s_and_b64 vcc, exec, s[40:41]
	s_nop 1
	v_permlane32_swap_b32 v16, v2
	s_waitcnt lgkmcnt(0)
	v_max_f32_e32 v16, v2, v16
	s_cbranch_vccz .LBB5_1036
	v_cmp_lt_f32_e32 vcc, s27, v16
	s_mov_b64 s[42:43], 0
	s_mov_b64 s[40:41], 0
	s_cbranch_vccz .LBB5_1027
	v_max_f32_e32 v2, v16, v16
	v_max_f32_e32 v2, 0, v2
	s_mov_b64 s[40:41], -1

; #define GAS __attribute__((address_space(1)))
; __device__ __forceinline__ void p11_combine(const P& p, int gw, int NGW, int lane, float oscale) {
;     ...
;     for (int m = gw; m < NTOK; m += NGW) {
;         GAS f32x4* xr = (GAS f32x4*)(p.out + (size_t)m * DM) + lane;
;         const GAS v2u* x2r = (const GAS v2u*)((const bf16*)(p.ws + WS_X2H) + (size_t)m * DM) + lane;
;         f32x4 a[8];
; #pragma unroll
;         for (int j = 0; j < 8; ++j) { const v2u w = x2r[64 * j]; a[j] = (f32x4){__uint_as_float(w.x << 16), __uint_as_float(w.x & 0xffff0000u), __uint_as_float(w.y << 16), __uint_as_float(w.y & 0xffff0000u)}; }
; #pragma unroll
;         for (int k = 0; k < TOPK; ++k) { const int e = tope[m * 4 + k]; const float g = topg[m * 4 + k]; const int slot = 256 * __shfl(toff_l, e) + tpos[m * 4 + k];
;             const GAS unsigned* yr = (const GAS unsigned*)(Y + (size_t)slot * DM) + lane;
; #pragma unroll
;             for (int j = 0; j < 8; ++j) { const int w = (int)yr[64 * j]; const f32x2 lo = __builtin_amdgcn_cvt_pk_f32_fp8(w, false), hi = __builtin_amdgcn_cvt_pk_f32_fp8(w, true);
;                 a[j].x += g * lo.x; a[j].y += g * lo.y; a[j].z += g * hi.x; a[j].w += g * hi.y; } }
.LBB5_1742:
	s_ashr_i32 s1, s0, 31
	s_lshl_b64 s[14:15], s[0:1], 2
	s_add_u32 s16, s6, s14
	s_addc_u32 s17, s7, s15
	global_load_dwordx2 v[36:37], v[20:21], off
	global_load_dwordx2 v[34:35], v[20:21], off offset:512
	global_load_dwordx2 v[32:33], v[20:21], off offset:1024
	global_load_dwordx2 v[30:31], v[20:21], off offset:1536
	global_load_dwordx2 v[28:29], v[20:21], off offset:2048
	global_load_dwordx2 v[26:27], v[20:21], off offset:2560
	global_load_dwordx2 v[24:25], v[20:21], off offset:3072
	global_load_dwordx2 v[22:23], v[20:21], off offset:3584
	global_load_dwordx4 v[46:49], v5, s[16:17]
	s_add_u32 s16, s8, s14
	s_addc_u32 s17, s9, s15
	s_add_u32 s14, s10, s14
	s_addc_u32 s15, s11, s15
	global_load_dword v54, v5, s[16:17]
	global_load_dword v53, v5, s[14:15]
	s_add_i32 s16, s0, 1
	s_ashr_i32 s17, s16, 31
	s_lshl_b64 s[14:15], s[16:17], 2
	s_add_u32 s16, s8, s14
	s_addc_u32 s17, s9, s15
	s_add_u32 s14, s10, s14
	s_addc_u32 s15, s11, s15
	global_load_dwordx3 v[50:52], v5, s[16:17]
	global_load_dword v55, v5, s[14:15]
	s_add_i32 s16, s0, 2
	s_ashr_i32 s17, s16, 31
	s_lshl_b64 s[14:15], s[16:17], 2
	s_add_u32 s14, s10, s14
	s_addc_u32 s15, s11, s15
	global_load_dwordx2 v[56:57], v5, s[14:15]
	global_load_dwordx4 v[0:3], v[6:7], off
	s_add_i32 s28, s28, s26
	s_add_i32 s0, s0, s12
	v_lshl_add_u64 v[20:21], v[20:21], 0, s[4:5]
	s_cmp_lt_i32 s28, 0x8000
	s_waitcnt vmcnt(14)
	v_lshlrev_b32_e32 v58, 16, v36
	v_and_b32_e32 v59, 0xffff0000, v36
	v_lshlrev_b32_e32 v36, 16, v37
	v_and_b32_e32 v37, 0xffff0000, v37
	s_waitcnt vmcnt(13)
	v_lshlrev_b32_e32 v60, 16, v34
	v_and_b32_e32 v61, 0xffff0000, v34
	v_lshlrev_b32_e32 v34, 16, v35
	v_and_b32_e32 v35, 0xffff0000, v35
	s_waitcnt vmcnt(6)
	v_and_or_b32 v46, v46, 63, v38
	v_lshlrev_b32_e32 v46, 2, v46
	v_and_or_b32 v47, v47, 63, v38
	ds_bpermute_b32 v46, v46, v39
	v_lshlrev_b32_e32 v47, 2, v47
	ds_bpermute_b32 v74, v47, v39
	v_and_or_b32 v48, v48, 63, v38
	v_and_or_b32 v49, v49, 63, v38
	v_lshlrev_b32_e32 v48, 2, v48
	s_waitcnt vmcnt(4) lgkmcnt(1)
	v_lshl_add_u32 v46, v46, 8, v53
	v_lshlrev_b32_e32 v49, 2, v49
	ds_bpermute_b32 v75, v48, v39
	v_ashrrev_i32_e32 v47, 31, v46
	ds_bpermute_b32 v49, v49, v39
	s_waitcnt vmcnt(3)
	v_mov_b32_e32 v48, v52
	v_lshlrev_b64 v[46:47], 11, v[46:47]
	s_waitcnt vmcnt(2) lgkmcnt(2)
	v_lshl_add_u32 v52, v74, 8, v55
	v_lshl_add_u64 v[46:47], v[16:17], 0, v[46:47]
	v_ashrrev_i32_e32 v53, 31, v52
	global_load_dword v55, v[46:47], off
	global_load_dword v74, v[46:47], off offset:256
	global_load_dword v78, v[46:47], off offset:512
	global_load_dword v82, v[46:47], off offset:768
	global_load_dword v86, v[46:47], off offset:1024
	global_load_dword v90, v[46:47], off offset:1280
	global_load_dword v94, v[46:47], off offset:1536
	global_load_dword v98, v[46:47], off offset:1792
	v_lshlrev_b64 v[46:47], 11, v[52:53]
	v_lshl_add_u64 v[46:47], v[16:17], 0, v[46:47]
	global_load_dword v102, v[46:47], off
	global_load_dword v106, v[46:47], off offset:256
	global_load_dword v110, v[46:47], off offset:512
	global_load_dword v114, v[46:47], off offset:768
	global_load_dword v118, v[46:47], off offset:1024
	global_load_dword v122, v[46:47], off offset:1280
	global_load_dword v126, v[46:47], off offset:1536
	global_load_dword v130, v[46:47], off offset:1792
	s_waitcnt vmcnt(17) lgkmcnt(1)
	v_lshl_add_u32 v46, v75, 8, v56
	s_waitcnt lgkmcnt(0)
	v_lshl_add_u32 v52, v49, 8, v57
	v_ashrrev_i32_e32 v47, 31, v46
	v_ashrrev_i32_e32 v53, 31, v52
	v_lshlrev_b64 v[46:47], 11, v[46:47]
	v_lshlrev_b64 v[52:53], 11, v[52:53]
	v_lshl_add_u64 v[46:47], v[16:17], 0, v[46:47]
	v_lshl_add_u64 v[52:53], v[16:17], 0, v[52:53]
	global_load_dword v49, v[46:47], off
	global_load_dword v132, v[46:47], off offset:256
	global_load_dword v133, v[46:47], off offset:512
	global_load_dword v134, v[46:47], off offset:768
	global_load_dword v135, v[46:47], off offset:1024
	global_load_dword v136, v[46:47], off offset:1280
	global_load_dword v137, v[46:47], off offset:1536
	global_load_dword v138, v[46:47], off offset:1792
	global_load_dword v139, v[52:53], off
	global_load_dword v140, v[52:53], off offset:256
	global_load_dword v141, v[52:53], off offset:512
	global_load_dword v142, v[52:53], off offset:768
	global_load_dword v143, v[52:53], off offset:1024
	global_load_dword v144, v[52:53], off offset:1280
	global_load_dword v145, v[52:53], off offset:1536
	global_load_dword v146, v[52:53], off offset:1792
	v_lshlrev_b32_e32 v62, 16, v32
	v_and_b32_e32 v63, 0xffff0000, v32
	v_lshlrev_b32_e32 v32, 16, v33
	v_and_b32_e32 v33, 0xffff0000, v33
	v_lshlrev_b32_e32 v64, 16, v30
	v_and_b32_e32 v65, 0xffff0000, v30
	v_lshlrev_b32_e32 v30, 16, v31
	v_and_b32_e32 v31, 0xffff0000, v31
	v_lshlrev_b32_e32 v66, 16, v28
	v_and_b32_e32 v67, 0xffff0000, v28
	v_lshlrev_b32_e32 v28, 16, v29
	v_and_b32_e32 v29, 0xffff0000, v29
	v_lshlrev_b32_e32 v68, 16, v26
	v_and_b32_e32 v69, 0xffff0000, v26
	v_lshlrev_b32_e32 v26, 16, v27
	v_and_b32_e32 v27, 0xffff0000, v27
	v_lshlrev_b32_e32 v70, 16, v24
	v_and_b32_e32 v71, 0xffff0000, v24
	v_lshlrev_b32_e32 v24, 16, v25
	v_and_b32_e32 v25, 0xffff0000, v25
	v_lshlrev_b32_e32 v72, 16, v22
	v_and_b32_e32 v73, 0xffff0000, v22
	v_lshlrev_b32_e32 v22, 16, v23
	v_and_b32_e32 v23, 0xffff0000, v23
	s_waitcnt vmcnt(31)
	v_cvt_pk_f32_fp8_e32 v[46:47], v55
	v_cvt_pk_f32_fp8_sdwa v[52:53], v55 src0_sel:WORD_1
	s_waitcnt vmcnt(30)
	v_cvt_pk_f32_fp8_e32 v[56:57], v74
	v_cvt_pk_f32_fp8_sdwa v[74:75], v74 src0_sel:WORD_1
	s_waitcnt vmcnt(29)
	v_cvt_pk_f32_fp8_e32 v[76:77], v78
	v_cvt_pk_f32_fp8_sdwa v[78:79], v78 src0_sel:WORD_1
	s_waitcnt vmcnt(28)
	v_cvt_pk_f32_fp8_e32 v[80:81], v82
	v_cvt_pk_f32_fp8_sdwa v[82:83], v82 src0_sel:WORD_1
	s_waitcnt vmcnt(27)
; #define GAS __attribute__((address_space(1)))
; __device__ __forceinline__ void p11_combine(const P& p, int gw, int NGW, int lane, float oscale) {
;     ...
;         for (int k = 0; k < TOPK; ++k) { const int e = tope[m * 4 + k]; const float g = topg[m * 4 + k]; const int slot = 256 * __shfl(toff_l, e) + tpos[m * 4 + k];
;             const GAS unsigned* yr = (const GAS unsigned*)(Y + (size_t)slot * DM) + lane;
; #pragma unroll
;             for (int j = 0; j < 8; ++j) { const int w = (int)yr[64 * j]; const f32x2 lo = __builtin_amdgcn_cvt_pk_f32_fp8(w, false), hi = __builtin_amdgcn_cvt_pk_f32_fp8(w, true);
;                 a[j].x += g * lo.x; a[j].y += g * lo.y; a[j].z += g * hi.x; a[j].w += g * hi.y; } }
	v_cvt_pk_f32_fp8_e32 v[84:85], v86
	v_cvt_pk_f32_fp8_sdwa v[86:87], v86 src0_sel:WORD_1
	s_waitcnt vmcnt(26)
	v_cvt_pk_f32_fp8_e32 v[88:89], v90
	v_cvt_pk_f32_fp8_sdwa v[90:91], v90 src0_sel:WORD_1
	s_waitcnt vmcnt(25)
	v_cvt_pk_f32_fp8_e32 v[92:93], v94
	v_cvt_pk_f32_fp8_sdwa v[94:95], v94 src0_sel:WORD_1
	s_waitcnt vmcnt(24)
	v_cvt_pk_f32_fp8_e32 v[96:97], v98
	v_cvt_pk_f32_fp8_sdwa v[98:99], v98 src0_sel:WORD_1
	s_waitcnt vmcnt(23)
	v_cvt_pk_f32_fp8_e32 v[100:101], v102
	v_cvt_pk_f32_fp8_sdwa v[102:103], v102 src0_sel:WORD_1
	s_waitcnt vmcnt(22)
	v_cvt_pk_f32_fp8_e32 v[104:105], v106
	v_cvt_pk_f32_fp8_sdwa v[106:107], v106 src0_sel:WORD_1
	s_waitcnt vmcnt(21)
	v_cvt_pk_f32_fp8_e32 v[108:109], v110
	s_waitcnt vmcnt(20)
	v_cvt_pk_f32_fp8_e32 v[112:113], v114
	s_waitcnt vmcnt(19)
	v_cvt_pk_f32_fp8_e32 v[116:117], v118
	s_waitcnt vmcnt(18)
	v_cvt_pk_f32_fp8_e32 v[120:121], v122
	s_waitcnt vmcnt(17)
	v_cvt_pk_f32_fp8_e32 v[124:125], v126
	v_cvt_pk_f32_fp8_sdwa v[110:111], v110 src0_sel:WORD_1
	v_cvt_pk_f32_fp8_sdwa v[114:115], v114 src0_sel:WORD_1
	v_cvt_pk_f32_fp8_sdwa v[118:119], v118 src0_sel:WORD_1
	v_cvt_pk_f32_fp8_sdwa v[122:123], v122 src0_sel:WORD_1
	v_cvt_pk_f32_fp8_sdwa v[126:127], v126 src0_sel:WORD_1
	s_waitcnt vmcnt(16)
	v_cvt_pk_f32_fp8_e32 v[128:129], v130
	v_cvt_pk_f32_fp8_sdwa v[130:131], v130 src0_sel:WORD_1
	v_pk_fma_f32 v[46:47], v[54:55], v[46:47], v[58:59] op_sel_hi:[0,1,1]
	v_pk_fma_f32 v[36:37], v[54:55], v[52:53], v[36:37] op_sel_hi:[0,1,1]
	v_pk_fma_f32 v[52:53], v[54:55], v[56:57], v[60:61] op_sel_hi:[0,1,1]
	v_pk_fma_f32 v[34:35], v[54:55], v[74:75], v[34:35] op_sel_hi:[0,1,1]
	v_pk_fma_f32 v[56:57], v[54:55], v[76:77], v[62:63] op_sel_hi:[0,1,1]
	v_pk_fma_f32 v[32:33], v[54:55], v[78:79], v[32:33] op_sel_hi:[0,1,1]
	v_pk_fma_f32 v[58:59], v[54:55], v[80:81], v[64:65] op_sel_hi:[0,1,1]
	v_pk_fma_f32 v[30:31], v[54:55], v[82:83], v[30:31] op_sel_hi:[0,1,1]
	v_pk_fma_f32 v[60:61], v[54:55], v[84:85], v[66:67] op_sel_hi:[0,1,1]
	v_pk_fma_f32 v[28:29], v[54:55], v[86:87], v[28:29] op_sel_hi:[0,1,1]
	v_pk_fma_f32 v[62:63], v[54:55], v[88:89], v[68:69] op_sel_hi:[0,1,1]
	v_pk_fma_f32 v[26:27], v[54:55], v[90:91], v[26:27] op_sel_hi:[0,1,1]
	v_pk_fma_f32 v[64:65], v[54:55], v[92:93], v[70:71] op_sel_hi:[0,1,1]
	v_pk_fma_f32 v[24:25], v[54:55], v[94:95], v[24:25] op_sel_hi:[0,1,1]
	v_pk_fma_f32 v[66:67], v[54:55], v[96:97], v[72:73] op_sel_hi:[0,1,1]
	v_pk_fma_f32 v[22:23], v[54:55], v[98:99], v[22:23] op_sel_hi:[0,1,1]
	s_waitcnt vmcnt(15)
	v_cvt_pk_f32_fp8_e32 v[54:55], v49
	v_cvt_pk_f32_fp8_sdwa v[68:69], v49 src0_sel:WORD_1
	s_waitcnt vmcnt(14)
	v_cvt_pk_f32_fp8_e32 v[70:71], v132
	v_cvt_pk_f32_fp8_sdwa v[72:73], v132 src0_sel:WORD_1
	s_waitcnt vmcnt(13)
	v_cvt_pk_f32_fp8_e32 v[74:75], v133
	v_cvt_pk_f32_fp8_sdwa v[76:77], v133 src0_sel:WORD_1
	s_waitcnt vmcnt(12)
	v_cvt_pk_f32_fp8_e32 v[78:79], v134
	v_cvt_pk_f32_fp8_sdwa v[80:81], v134 src0_sel:WORD_1
	s_waitcnt vmcnt(11)
	v_cvt_pk_f32_fp8_e32 v[82:83], v135
	v_cvt_pk_f32_fp8_sdwa v[84:85], v135 src0_sel:WORD_1
	s_waitcnt vmcnt(10)
	v_cvt_pk_f32_fp8_e32 v[86:87], v136
	v_cvt_pk_f32_fp8_sdwa v[88:89], v136 src0_sel:WORD_1
	s_waitcnt vmcnt(9)
	v_cvt_pk_f32_fp8_e32 v[90:91], v137
	v_cvt_pk_f32_fp8_sdwa v[92:93], v137 src0_sel:WORD_1
	s_waitcnt vmcnt(8)
	v_cvt_pk_f32_fp8_e32 v[94:95], v138
	v_cvt_pk_f32_fp8_sdwa v[96:97], v138 src0_sel:WORD_1
	s_waitcnt vmcnt(7)
	v_cvt_pk_f32_fp8_e32 v[98:99], v139
	v_cvt_pk_f32_fp8_sdwa v[132:133], v139 src0_sel:WORD_1
	v_pk_fma_f32 v[46:47], v[50:51], v[100:101], v[46:47] op_sel_hi:[0,1,1]
	v_pk_fma_f32 v[36:37], v[50:51], v[102:103], v[36:37] op_sel_hi:[0,1,1]
	s_waitcnt vmcnt(6)
	v_cvt_pk_f32_fp8_e32 v[100:101], v140
	v_cvt_pk_f32_fp8_sdwa v[102:103], v140 src0_sel:WORD_1
	v_pk_fma_f32 v[52:53], v[50:51], v[104:105], v[52:53] op_sel_hi:[0,1,1]
	v_pk_fma_f32 v[34:35], v[50:51], v[106:107], v[34:35] op_sel_hi:[0,1,1]
	s_waitcnt vmcnt(5)
	v_cvt_pk_f32_fp8_e32 v[104:105], v141
	v_cvt_pk_f32_fp8_sdwa v[106:107], v141 src0_sel:WORD_1
	v_pk_fma_f32 v[56:57], v[50:51], v[108:109], v[56:57] op_sel_hi:[0,1,1]
	s_waitcnt vmcnt(4)
	v_cvt_pk_f32_fp8_e32 v[108:109], v142
	v_pk_fma_f32 v[58:59], v[50:51], v[112:113], v[58:59] op_sel_hi:[0,1,1]
	s_waitcnt vmcnt(3)
	v_cvt_pk_f32_fp8_e32 v[112:113], v143
	v_pk_fma_f32 v[60:61], v[50:51], v[116:117], v[60:61] op_sel_hi:[0,1,1]
	s_waitcnt vmcnt(2)
	v_cvt_pk_f32_fp8_e32 v[116:117], v144
	v_pk_fma_f32 v[62:63], v[50:51], v[120:121], v[62:63] op_sel_hi:[0,1,1]
	s_waitcnt vmcnt(1)
	v_cvt_pk_f32_fp8_e32 v[120:121], v145
	v_pk_fma_f32 v[64:65], v[50:51], v[124:125], v[64:65] op_sel_hi:[0,1,1]
	s_waitcnt vmcnt(0)
; #define GAS __attribute__((address_space(1)))
; __device__ __forceinline__ void p11_combine(const P& p, int gw, int NGW, int lane, float oscale) {
;     ...
;         for (int k = 0; k < TOPK; ++k) { const int e = tope[m * 4 + k]; const float g = topg[m * 4 + k]; const int slot = 256 * __shfl(toff_l, e) + tpos[m * 4 + k];
;             const GAS unsigned* yr = (const GAS unsigned*)(Y + (size_t)slot * DM) + lane;
; #pragma unroll
;             for (int j = 0; j < 8; ++j) { const int w = (int)yr[64 * j]; const f32x2 lo = __builtin_amdgcn_cvt_pk_f32_fp8(w, false), hi = __builtin_amdgcn_cvt_pk_f32_fp8(w, true);
;                 a[j].x += g * lo.x; a[j].y += g * lo.y; a[j].z += g * hi.x; a[j].w += g * hi.y; } }
;         float ss = 0.f;
; #pragma unroll
;         for (int j = 0; j < 8; ++j) ss += (a[j].x * a[j].x + a[j].y * a[j].y) + (a[j].z * a[j].z + a[j].w * a[j].w);
	v_cvt_pk_f32_fp8_e32 v[124:125], v146
	v_pk_fma_f32 v[32:33], v[50:51], v[110:111], v[32:33] op_sel_hi:[0,1,1]
	v_cvt_pk_f32_fp8_sdwa v[110:111], v142 src0_sel:WORD_1
	v_pk_fma_f32 v[30:31], v[50:51], v[114:115], v[30:31] op_sel_hi:[0,1,1]
	v_cvt_pk_f32_fp8_sdwa v[114:115], v143 src0_sel:WORD_1
	v_pk_fma_f32 v[28:29], v[50:51], v[118:119], v[28:29] op_sel_hi:[0,1,1]
	v_cvt_pk_f32_fp8_sdwa v[118:119], v144 src0_sel:WORD_1
	v_pk_fma_f32 v[26:27], v[50:51], v[122:123], v[26:27] op_sel_hi:[0,1,1]
	v_cvt_pk_f32_fp8_sdwa v[122:123], v145 src0_sel:WORD_1
	v_pk_fma_f32 v[24:25], v[50:51], v[126:127], v[24:25] op_sel_hi:[0,1,1]
	v_cvt_pk_f32_fp8_sdwa v[126:127], v146 src0_sel:WORD_1
	v_pk_fma_f32 v[66:67], v[50:51], v[128:129], v[66:67] op_sel_hi:[0,1,1]
	v_pk_fma_f32 v[22:23], v[50:51], v[130:131], v[22:23] op_sel_hi:[0,1,1]
	v_pk_fma_f32 v[46:47], v[50:51], v[54:55], v[46:47] op_sel:[1,0,0]
	v_pk_fma_f32 v[36:37], v[50:51], v[68:69], v[36:37] op_sel:[1,0,0]
	v_pk_fma_f32 v[52:53], v[50:51], v[70:71], v[52:53] op_sel:[1,0,0]
	v_pk_fma_f32 v[34:35], v[50:51], v[72:73], v[34:35] op_sel:[1,0,0]
	v_pk_fma_f32 v[54:55], v[50:51], v[74:75], v[56:57] op_sel:[1,0,0]
	v_pk_fma_f32 v[32:33], v[50:51], v[76:77], v[32:33] op_sel:[1,0,0]
	v_pk_fma_f32 v[56:57], v[50:51], v[78:79], v[58:59] op_sel:[1,0,0]
	v_pk_fma_f32 v[30:31], v[50:51], v[80:81], v[30:31] op_sel:[1,0,0]
	v_pk_fma_f32 v[58:59], v[50:51], v[82:83], v[60:61] op_sel:[1,0,0]
	v_pk_fma_f32 v[28:29], v[50:51], v[84:85], v[28:29] op_sel:[1,0,0]
	v_pk_fma_f32 v[60:61], v[50:51], v[86:87], v[62:63] op_sel:[1,0,0]
	v_pk_fma_f32 v[26:27], v[50:51], v[88:89], v[26:27] op_sel:[1,0,0]
	v_pk_fma_f32 v[62:63], v[50:51], v[90:91], v[64:65] op_sel:[1,0,0]
	v_pk_fma_f32 v[24:25], v[50:51], v[92:93], v[24:25] op_sel:[1,0,0]
	v_pk_fma_f32 v[64:65], v[50:51], v[94:95], v[66:67] op_sel:[1,0,0]
	v_pk_fma_f32 v[22:23], v[50:51], v[96:97], v[22:23] op_sel:[1,0,0]
	v_pk_fma_f32 v[46:47], v[48:49], v[98:99], v[46:47] op_sel_hi:[0,1,1]
	v_pk_fma_f32 v[36:37], v[48:49], v[132:133], v[36:37] op_sel_hi:[0,1,1]
	v_pk_fma_f32 v[50:51], v[48:49], v[100:101], v[52:53] op_sel_hi:[0,1,1]
	v_pk_fma_f32 v[34:35], v[48:49], v[102:103], v[34:35] op_sel_hi:[0,1,1]
	v_pk_fma_f32 v[52:53], v[48:49], v[104:105], v[54:55] op_sel_hi:[0,1,1]
	v_pk_fma_f32 v[32:33], v[48:49], v[106:107], v[32:33] op_sel_hi:[0,1,1]
	v_pk_fma_f32 v[54:55], v[48:49], v[108:109], v[56:57] op_sel_hi:[0,1,1]
	v_pk_fma_f32 v[56:57], v[48:49], v[112:113], v[58:59] op_sel_hi:[0,1,1]
	v_pk_fma_f32 v[58:59], v[48:49], v[116:117], v[60:61] op_sel_hi:[0,1,1]
	v_pk_fma_f32 v[60:61], v[48:49], v[120:121], v[62:63] op_sel_hi:[0,1,1]
	v_pk_fma_f32 v[62:63], v[48:49], v[124:125], v[64:65] op_sel_hi:[0,1,1]
	v_mov_b32_e32 v64, v47
	v_mov_b32_e32 v65, v51
	v_mov_b32_e32 v68, v37
	v_mov_b32_e32 v69, v35
	v_pk_fma_f32 v[30:31], v[48:49], v[110:111], v[30:31] op_sel_hi:[0,1,1]
	v_pk_fma_f32 v[28:29], v[48:49], v[114:115], v[28:29] op_sel_hi:[0,1,1]
	v_pk_fma_f32 v[26:27], v[48:49], v[118:119], v[26:27] op_sel_hi:[0,1,1]
	v_pk_fma_f32 v[24:25], v[48:49], v[122:123], v[24:25] op_sel_hi:[0,1,1]
	v_pk_fma_f32 v[22:23], v[48:49], v[126:127], v[22:23] op_sel_hi:[0,1,1]
	v_mov_b32_e32 v48, v46
	v_mov_b32_e32 v49, v50
	v_mov_b32_e32 v66, v36
	v_mov_b32_e32 v67, v34
	v_mov_b32_e32 v72, v53
	v_mov_b32_e32 v73, v33
	v_pk_mul_f32 v[64:65], v[64:65], v[64:65]
	v_pk_mul_f32 v[68:69], v[68:69], v[68:69]
	v_mov_b32_e32 v70, v52
	v_mov_b32_e32 v71, v32
	v_pk_mul_f32 v[72:73], v[72:73], v[72:73]
	v_pk_fma_f32 v[48:49], v[48:49], v[48:49], v[64:65]
	v_pk_fma_f32 v[64:65], v[66:67], v[66:67], v[68:69]
	v_mul_f32_e32 v74, v55, v55
	v_mul_f32_e32 v76, v31, v31
	v_pk_fma_f32 v[66:67], v[70:71], v[70:71], v[72:73]
	v_pk_add_f32 v[48:49], v[48:49], v[64:65]
	v_pk_mul_f32 v[78:79], v[56:57], v[56:57]
	v_pk_mul_f32 v[80:81], v[28:29], v[28:29]
	v_pk_fma_f32 v[74:75], v[54:55], v[54:55], v[74:75] op_sel_hi:[1,1,0]
	v_pk_fma_f32 v[76:77], v[30:31], v[30:31], v[76:77] op_sel_hi:[1,1,0]
	v_pk_add_f32 v[64:65], v[66:67], v[66:67] op_sel:[0,1] op_sel_hi:[1,0]
	v_pk_add_f32 v[48:49], v[48:49], v[48:49] op_sel:[0,1] op_sel_hi:[1,0]
; #define GAS __attribute__((address_space(1)))
; __device__ __forceinline__ void p11_combine(const P& p, int gw, int NGW, int lane, float oscale) {
;     ...
;         float ss = 0.f;
; #pragma unroll
;         for (int j = 0; j < 8; ++j) ss += (a[j].x * a[j].x + a[j].y * a[j].y) + (a[j].z * a[j].z + a[j].w * a[j].w);
;         ss = wave_sum(ss); const float r = rsqrtf(ss * (1.0f / DM) + EPS) * oscale;
;         const GAS f32x4* gf = (const GAS f32x4*)p.g_fin + lane;
; #pragma unroll
;         for (int j = 0; j < 8; ++j) { const f32x4 g = gf[64 * j]; xr[64 * j] = a[j] * r * g; }
	v_mov_b32_e32 v84, v59
	v_mov_b32_e32 v85, v27
	v_mov_b32_e32 v75, v80
	v_mov_b32_e32 v77, v81
	v_mov_b32_e32 v65, v79
	v_mov_b32_e32 v49, v78
	v_mov_b32_e32 v82, v58
	v_mov_b32_e32 v83, v26
	v_pk_mul_f32 v[84:85], v[84:85], v[84:85]
	v_pk_add_f32 v[66:67], v[74:75], v[76:77]
	v_pk_add_f32 v[48:49], v[48:49], v[64:65]
	v_mul_f32_e32 v86, v61, v61
	v_mul_f32_e32 v88, v25, v25
	v_pk_fma_f32 v[68:69], v[82:83], v[82:83], v[84:85]
	v_pk_add_f32 v[48:49], v[48:49], v[66:67]
	v_pk_mul_f32 v[90:91], v[62:63], v[62:63]
	v_pk_mul_f32 v[92:93], v[22:23], v[22:23]
	v_pk_fma_f32 v[86:87], v[60:61], v[60:61], v[86:87] op_sel_hi:[1,1,0]
	v_pk_fma_f32 v[88:89], v[24:25], v[24:25], v[88:89] op_sel_hi:[1,1,0]
	v_pk_add_f32 v[68:69], v[68:69], v[68:69] op_sel:[0,1] op_sel_hi:[1,0]
	v_pk_add_f32 v[48:49], v[48:49], v[48:49] op_sel:[0,1] op_sel_hi:[1,0]
	v_mov_b32_e32 v87, v92
	v_mov_b32_e32 v89, v93
	v_mov_b32_e32 v69, v91
	v_mov_b32_e32 v49, v90
	v_pk_add_f32 v[70:71], v[86:87], v[88:89]
	v_pk_add_f32 v[48:49], v[48:49], v[68:69]
	s_nop 0
	v_pk_add_f32 v[48:49], v[48:49], v[70:71]
	s_nop 0
	v_add_f32_e32 v48, v48, v49
	s_nop 1
	v_add_f32_dpp v48, v48, v48 quad_perm:[1,0,3,2] row_mask:0xf bank_mask:0xf
	s_nop 1
	v_add_f32_dpp v48, v48, v48 quad_perm:[2,3,0,1] row_mask:0xf bank_mask:0xf
	s_nop 1
	v_add_f32_dpp v48, v48, v48 row_half_mirror row_mask:0xf bank_mask:0xf
	s_nop 1
	v_add_f32_dpp v48, v48, v48 row_mirror row_mask:0xf bank_mask:0xf
	v_mov_b32_e32 v49, v48
	s_nop 1
	v_permlane16_swap_b32 v49, v48
	v_add_f32_e32 v48, v48, v49
	v_mov_b32_e32 v49, v48
	s_nop 1
	v_permlane32_swap_b32 v49, v48
	v_add_f32_e32 v48, v48, v49
	v_fmamk_f32 v48, v48, 0x3a000000, v4
	v_mul_f32_e32 v49, 0x4b800000, v48
	v_cmp_gt_f32_e32 vcc, s13, v48
	s_nop 1
	v_cndmask_b32_e32 v48, v48, v49, vcc
	v_rsq_f32_e32 v48, v48
	s_nop 0
	v_mul_f32_e32 v49, 0x45800000, v48
	v_cndmask_b32_e32 v48, v48, v49, vcc
	v_pk_mul_f32 v[46:47], v[46:47], v[48:49] op_sel_hi:[1,0]
	v_pk_mul_f32 v[36:37], v[36:37], v[48:49] op_sel_hi:[1,0]
	v_pk_mul_f32 v[0:1], v[0:1], v[46:47]
	v_pk_mul_f32 v[2:3], v[2:3], v[36:37]
	global_store_dwordx4 v[18:19], v[0:3], off offset:-4096
	v_pk_mul_f32 v[34:35], v[34:35], v[48:49] op_sel_hi:[1,0]
	v_pk_mul_f32 v[36:37], v[50:51], v[48:49] op_sel_hi:[1,0]
	v_pk_mul_f32 v[32:33], v[32:33], v[48:49] op_sel_hi:[1,0]
	v_pk_mul_f32 v[30:31], v[30:31], v[48:49] op_sel_hi:[1,0]
	v_pk_mul_f32 v[28:29], v[28:29], v[48:49] op_sel_hi:[1,0]
	v_pk_mul_f32 v[26:27], v[26:27], v[48:49] op_sel_hi:[1,0]
	v_pk_mul_f32 v[24:25], v[24:25], v[48:49] op_sel_hi:[1,0]
	v_pk_mul_f32 v[22:23], v[22:23], v[48:49] op_sel_hi:[1,0]
	v_pk_mul_f32 v[192:193], v[164:165], v[36:37]
	v_pk_mul_f32 v[194:195], v[166:167], v[34:35]
	global_store_dwordx4 v[18:19], v[192:195], off offset:-3072
	v_pk_mul_f32 v[34:35], v[52:53], v[48:49] op_sel_hi:[1,0]
	v_pk_mul_f32 v[2:3], v[170:171], v[32:33]
	v_pk_mul_f32 v[0:1], v[168:169], v[34:35]
	global_store_dwordx4 v[18:19], v[0:3], off offset:-2048
	v_pk_mul_f32 v[32:33], v[54:55], v[48:49] op_sel_hi:[1,0]
	v_pk_mul_f32 v[194:195], v[174:175], v[30:31]
	v_pk_mul_f32 v[192:193], v[172:173], v[32:33]
	global_store_dwordx4 v[18:19], v[192:195], off offset:-1024
	v_pk_mul_f32 v[30:31], v[56:57], v[48:49] op_sel_hi:[1,0]
	v_pk_mul_f32 v[2:3], v[178:179], v[28:29]
	v_pk_mul_f32 v[0:1], v[176:177], v[30:31]
	global_store_dwordx4 v[18:19], v[0:3], off
	v_pk_mul_f32 v[28:29], v[58:59], v[48:49] op_sel_hi:[1,0]
	v_pk_mul_f32 v[194:195], v[182:183], v[26:27]
	v_pk_mul_f32 v[192:193], v[180:181], v[28:29]
	global_store_dwordx4 v[18:19], v[192:195], off offset:1024
	v_pk_mul_f32 v[26:27], v[60:61], v[48:49] op_sel_hi:[1,0]
	v_pk_mul_f32 v[2:3], v[186:187], v[24:25]
	v_pk_mul_f32 v[0:1], v[184:185], v[26:27]
	global_store_dwordx4 v[18:19], v[0:3], off offset:2048
	v_pk_mul_f32 v[24:25], v[62:63], v[48:49] op_sel_hi:[1,0]
	v_pk_mul_f32 v[194:195], v[190:191], v[22:23]
	v_pk_mul_f32 v[192:193], v[188:189], v[24:25]
	global_store_dwordx4 v[18:19], v[192:195], off offset:3072
	v_lshl_add_u64 v[18:19], v[18:19], 0, s[2:3]
	s_cbranch_scc1 .LBB5_1742
